# v41
# speedup vs baseline: 1.0009x; 1.0009x over previous
.LBB2_71:
	s_or_b64 exec, exec, s[0:1]
	v_lshlrev_b32_e32 v14, 2, v72
	v_lshlrev_b32_e32 v10, 4, v73
	v_or_b32_e32 v12, v14, v1
	s_movk_i32 s8, 0x110
	v_mad_u32_u24 v2, v12, s8, v10
	s_waitcnt lgkmcnt(0)
	s_barrier
	ds_read_b128 v[2:5], v2
	v_mov_b32_e32 v67, 0
	v_mov_b32_e32 v11, v67
	v_lshl_add_u64 v[8:9], s[4:5], 0, v[10:11]
	v_add_u32_e32 v12, s18, v12
	s_waitcnt lgkmcnt(0)
	v_cvt_f32_f16_e32 v13, v2
	v_cvt_f32_f16_sdwa v15, v2 dst_sel:DWORD dst_unused:UNUSED_PAD src0_sel:WORD_1
	v_cvt_f32_f16_e32 v16, v3
	v_cvt_f32_f16_sdwa v17, v3 dst_sel:DWORD dst_unused:UNUSED_PAD src0_sel:WORD_1
	v_cvt_f32_f16_e32 v19, v4
	v_cvt_f32_f16_sdwa v20, v4 dst_sel:DWORD dst_unused:UNUSED_PAD src0_sel:WORD_1
	v_cvt_f32_f16_e32 v21, v5
	v_cvt_f32_f16_sdwa v22, v5 dst_sel:DWORD dst_unused:UNUSED_PAD src0_sel:WORD_1
	v_max3_f32 v11, v13, 0, v15
	v_max3_f32 v11, v11, v16, v17
	v_max3_f32 v11, v11, v19, v20
	v_max3_f32 v11, v11, v21, v22
	v_cmp_ne_u32_e64 s[0:1], 15, v72
	s_mov_b32 s4, 0x186a0
	v_mov_b32_dpp v18, v11 quad_perm:[1,0,3,2] row_mask:0xf bank_mask:0xf bound_ctrl:1
	v_max_f32_e32 v18, v18, v18
	v_max_f32_e32 v11, v11, v18
	v_lshl_add_u64 v[6:7], s[6:7], 0, v[66:67]
	v_cmp_eq_u32_e32 vcc, 0, v73
	v_mov_b32_dpp v18, v11 quad_perm:[2,3,0,1] row_mask:0xf bank_mask:0xf bound_ctrl:1
	v_max_f32_e32 v18, v18, v18
	v_max_f32_e32 v11, v11, v18
	s_nop 1
	v_mov_b32_dpp v18, v11 row_half_mirror row_mask:0xf bank_mask:0xf bound_ctrl:1
	v_max_f32_e32 v18, v18, v18
	v_max_f32_e32 v18, v11, v18
	v_mov_b32_e32 v11, 0x186a0
	v_cndmask_b32_e64 v12, v11, v12, s[0:1]
	v_mov_b32_dpp v23, v18 row_mirror row_mask:0xf bank_mask:0xf bound_ctrl:1
	v_cmp_gt_i32_e64 s[0:1], s4, v12
	s_and_saveexec_b64 s[2:3], s[0:1]
	s_cbranch_execz .LBB2_74
	v_max_f32_e32 v23, v23, v23
	v_max_f32_e32 v18, v18, v18
	v_max_f32_e32 v18, v18, v23
	v_rcp_f32_e32 v23, v18
	v_cmp_lt_f32_e64 s[0:1], 0, v18
	v_mul_f32_e32 v23, 0x437f0000, v23
	s_nop 0
	v_cndmask_b32_e64 v23, 0, v23, s[0:1]
	v_mul_f32_e32 v13, v23, v13
	v_mul_f32_e32 v19, v23, v19
	v_mul_f32_e32 v15, v23, v15
	v_rndne_f32_e32 v13, v13
	v_mul_f32_e32 v20, v23, v20
	v_rndne_f32_e32 v19, v19
	v_mul_f32_e32 v16, v23, v16
	v_rndne_f32_e32 v15, v15
	v_cvt_pk_u8_f32 v13, v13, 0, 0
	v_mul_f32_e32 v21, v23, v21
	v_rndne_f32_e32 v20, v20
	v_cvt_pk_u8_f32 v19, v19, 0, 0
	v_mul_f32_e32 v17, v23, v17
	v_rndne_f32_e32 v16, v16
	v_cvt_pk_u8_f32 v13, v15, 1, v13
	v_mul_f32_e32 v22, v23, v22
	v_rndne_f32_e32 v21, v21
	v_cvt_pk_u8_f32 v19, v20, 1, v19
	v_rndne_f32_e32 v17, v17
	v_cvt_pk_u8_f32 v13, v16, 2, v13
	v_rndne_f32_e32 v22, v22
	v_cvt_pk_u8_f32 v19, v21, 2, v19
	v_cvt_pk_u8_f32 v20, v17, 3, v13
	v_ashrrev_i32_e32 v13, 31, v12
	v_cvt_pk_u8_f32 v21, v22, 3, v19
	v_lshlrev_b64 v[22:23], 8, v[12:13]
	v_lshlrev_b64 v[16:17], 7, v[12:13]
	v_lshl_add_u64 v[22:23], v[8:9], 0, v[22:23]
	global_store_dwordx4 v[22:23], v[2:5], off sc1
	s_nop 1
	v_lshl_add_u64 v[2:3], v[6:7], 0, v[16:17]
	global_store_dwordx2 v[2:3], v[20:21], off
	s_and_b64 exec, exec, vcc
	s_cbranch_execz .LBB2_74
	v_lshl_add_u64 v[2:3], v[12:13], 2, s[14:15]
	v_mul_f32_e32 v4, 0x40808081, v18
	global_store_dword v[2:3], v4, off
.LBB2_74:
	s_or_b64 exec, exec, s[2:3]
	v_add3_u32 v12, v14, v1, 16
	v_mad_u32_u24 v2, v12, s8, v10
	ds_read_b128 v[2:5], v2
	s_movk_i32 s0, 0x2c0
	v_add_u32_e32 v12, s18, v12
	v_cmp_gt_u32_e64 s[0:1], s0, v0
	s_waitcnt lgkmcnt(0)
	v_cvt_f32_f16_e32 v13, v2
	v_cvt_f32_f16_sdwa v15, v2 dst_sel:DWORD dst_unused:UNUSED_PAD src0_sel:WORD_1
	v_cvt_f32_f16_e32 v16, v3
	v_cvt_f32_f16_sdwa v17, v3 dst_sel:DWORD dst_unused:UNUSED_PAD src0_sel:WORD_1
	v_cvt_f32_f16_e32 v18, v4
	v_cvt_f32_f16_sdwa v19, v4 dst_sel:DWORD dst_unused:UNUSED_PAD src0_sel:WORD_1
	v_cvt_f32_f16_e32 v20, v5
	v_cvt_f32_f16_sdwa v21, v5 dst_sel:DWORD dst_unused:UNUSED_PAD src0_sel:WORD_1
	v_max3_f32 v22, v13, 0, v15
	v_max3_f32 v22, v22, v16, v17
	v_max3_f32 v22, v22, v18, v19
	v_max3_f32 v22, v22, v20, v21
	v_cndmask_b32_e64 v12, v11, v12, s[0:1]
	v_cmp_gt_i32_e64 s[0:1], s4, v12
	v_mov_b32_dpp v23, v22 quad_perm:[1,0,3,2] row_mask:0xf bank_mask:0xf bound_ctrl:1
	v_max_f32_e32 v23, v23, v23
	v_max_f32_e32 v22, v22, v23
	s_nop 1
	v_mov_b32_dpp v23, v22 quad_perm:[2,3,0,1] row_mask:0xf bank_mask:0xf bound_ctrl:1
	v_max_f32_e32 v23, v23, v23
	v_max_f32_e32 v22, v22, v23
	s_nop 1
	v_mov_b32_dpp v23, v22 row_half_mirror row_mask:0xf bank_mask:0xf bound_ctrl:1
	v_max_f32_e32 v23, v23, v23
	v_max_f32_e32 v22, v22, v23
	s_nop 1
	v_mov_b32_dpp v23, v22 row_mirror row_mask:0xf bank_mask:0xf bound_ctrl:1
	s_and_saveexec_b64 s[2:3], s[0:1]
	s_cbranch_execz .LBB2_77
	v_max_f32_e32 v11, v23, v23
	v_max_f32_e32 v22, v22, v22
	v_max_f32_e32 v11, v22, v11
	v_rcp_f32_e32 v22, v11
	v_cmp_lt_f32_e64 s[0:1], 0, v11
	v_mul_f32_e32 v22, 0x437f0000, v22
	s_nop 0
	v_cndmask_b32_e64 v22, 0, v22, s[0:1]
	v_mul_f32_e32 v18, v22, v18
	v_mul_f32_e32 v13, v22, v13
	v_mul_f32_e32 v19, v22, v19
	v_rndne_f32_e32 v18, v18
	v_mul_f32_e32 v15, v22, v15
	v_rndne_f32_e32 v13, v13
	v_mul_f32_e32 v20, v22, v20
	v_rndne_f32_e32 v19, v19
	v_cvt_pk_u8_f32 v18, v18, 0, 0
	v_mul_f32_e32 v16, v22, v16
	v_rndne_f32_e32 v15, v15
	v_cvt_pk_u8_f32 v13, v13, 0, 0
	v_mul_f32_e32 v21, v22, v21
	v_rndne_f32_e32 v20, v20
	v_cvt_pk_u8_f32 v18, v19, 1, v18
	v_mul_f32_e32 v17, v22, v17
	v_rndne_f32_e32 v16, v16
	v_cvt_pk_u8_f32 v13, v15, 1, v13
	v_rndne_f32_e32 v21, v21
	v_cvt_pk_u8_f32 v18, v20, 2, v18
	v_rndne_f32_e32 v17, v17
	v_cvt_pk_u8_f32 v13, v16, 2, v13
	v_cvt_pk_u8_f32 v19, v21, 3, v18
	v_cvt_pk_u8_f32 v18, v17, 3, v13
	v_ashrrev_i32_e32 v13, 31, v12
	v_lshlrev_b64 v[20:21], 8, v[12:13]
	v_lshlrev_b64 v[16:17], 7, v[12:13]
	v_lshl_add_u64 v[20:21], v[8:9], 0, v[20:21]
	global_store_dwordx4 v[20:21], v[2:5], off sc1
	s_nop 1
	v_lshl_add_u64 v[2:3], v[6:7], 0, v[16:17]
	global_store_dwordx2 v[2:3], v[18:19], off
	s_and_b64 exec, exec, vcc
	s_cbranch_execz .LBB2_77
	v_lshl_add_u64 v[2:3], v[12:13], 2, s[14:15]
	v_mul_f32_e32 v4, 0x40808081, v11
	global_store_dword v[2:3], v4, off
.LBB2_77:
	s_or_b64 exec, exec, s[2:3]
	v_add_u32_e32 v2, v14, v1
	v_or_b32_e32 v11, 32, v2
	s_movk_i32 s5, 0x110
	v_mad_u32_u24 v2, v11, s5, v10
	ds_read_b128 v[2:5], v2
	v_add_u32_e32 v12, s18, v11
	s_movk_i32 s0, 0x1c0
	v_cmp_gt_u32_e64 s[0:1], s0, v0
	s_waitcnt lgkmcnt(0)
	v_cvt_f32_f16_e32 v13, v2
	v_cvt_f32_f16_sdwa v15, v2 dst_sel:DWORD dst_unused:UNUSED_PAD src0_sel:WORD_1
	v_cvt_f32_f16_e32 v16, v3
	v_cvt_f32_f16_sdwa v17, v3 dst_sel:DWORD dst_unused:UNUSED_PAD src0_sel:WORD_1
	v_cvt_f32_f16_e32 v19, v4
	v_cvt_f32_f16_sdwa v20, v4 dst_sel:DWORD dst_unused:UNUSED_PAD src0_sel:WORD_1
	v_cvt_f32_f16_e32 v21, v5
	v_cvt_f32_f16_sdwa v22, v5 dst_sel:DWORD dst_unused:UNUSED_PAD src0_sel:WORD_1
	v_max3_f32 v11, v13, 0, v15
	v_max3_f32 v11, v11, v16, v17
	v_max3_f32 v11, v11, v19, v20
	v_max3_f32 v11, v11, v21, v22
	s_nop 1
	v_mov_b32_dpp v18, v11 quad_perm:[1,0,3,2] row_mask:0xf bank_mask:0xf bound_ctrl:1
	v_max_f32_e32 v18, v18, v18
	v_max_f32_e32 v11, v11, v18
	s_nop 1
	v_mov_b32_dpp v18, v11 quad_perm:[2,3,0,1] row_mask:0xf bank_mask:0xf bound_ctrl:1
	v_max_f32_e32 v18, v18, v18
	v_max_f32_e32 v11, v11, v18
	s_nop 1
	v_mov_b32_dpp v18, v11 row_half_mirror row_mask:0xf bank_mask:0xf bound_ctrl:1
	v_max_f32_e32 v18, v18, v18
	v_max_f32_e32 v18, v11, v18
	v_mov_b32_e32 v11, 0x186a0
	v_cndmask_b32_e64 v12, v11, v12, s[0:1]
	v_mov_b32_dpp v23, v18 row_mirror row_mask:0xf bank_mask:0xf bound_ctrl:1
	v_cmp_gt_i32_e64 s[0:1], s4, v12
	s_and_saveexec_b64 s[2:3], s[0:1]
	s_cbranch_execz .LBB2_80
	v_max_f32_e32 v23, v23, v23
	v_max_f32_e32 v18, v18, v18
	v_max_f32_e32 v18, v18, v23
	v_rcp_f32_e32 v23, v18
	v_cmp_lt_f32_e64 s[0:1], 0, v18
	v_mul_f32_e32 v23, 0x437f0000, v23
	s_nop 0
	v_cndmask_b32_e64 v23, 0, v23, s[0:1]
	v_mul_f32_e32 v13, v23, v13
	v_mul_f32_e32 v19, v23, v19
	v_mul_f32_e32 v15, v23, v15
	v_rndne_f32_e32 v13, v13
	v_mul_f32_e32 v20, v23, v20
	v_rndne_f32_e32 v19, v19
	v_mul_f32_e32 v16, v23, v16
	v_rndne_f32_e32 v15, v15
	v_cvt_pk_u8_f32 v13, v13, 0, 0
	v_mul_f32_e32 v21, v23, v21
	v_rndne_f32_e32 v20, v20
	v_cvt_pk_u8_f32 v19, v19, 0, 0
	v_mul_f32_e32 v17, v23, v17
	v_rndne_f32_e32 v16, v16
	v_cvt_pk_u8_f32 v13, v15, 1, v13
	v_mul_f32_e32 v22, v23, v22
	v_rndne_f32_e32 v21, v21
	v_cvt_pk_u8_f32 v19, v20, 1, v19
	v_rndne_f32_e32 v17, v17
	v_cvt_pk_u8_f32 v13, v16, 2, v13
	v_rndne_f32_e32 v22, v22
	v_cvt_pk_u8_f32 v19, v21, 2, v19
	v_cvt_pk_u8_f32 v20, v17, 3, v13
	v_ashrrev_i32_e32 v13, 31, v12
	v_cvt_pk_u8_f32 v21, v22, 3, v19
	v_lshlrev_b64 v[22:23], 8, v[12:13]
	v_lshlrev_b64 v[16:17], 7, v[12:13]
	v_lshl_add_u64 v[22:23], v[8:9], 0, v[22:23]
	global_store_dwordx4 v[22:23], v[2:5], off sc1
	s_nop 1
	v_lshl_add_u64 v[2:3], v[6:7], 0, v[16:17]
	global_store_dwordx2 v[2:3], v[20:21], off
	s_and_b64 exec, exec, vcc
	s_cbranch_execz .LBB2_80
	v_lshl_add_u64 v[2:3], v[12:13], 2, s[14:15]
	v_mul_f32_e32 v4, 0x40808081, v18
	global_store_dword v[2:3], v4, off
.LBB2_80:
	s_or_b64 exec, exec, s[2:3]
	v_add3_u32 v1, v14, v1, 48
	v_min_i32_e32 v2, 59, v1
	v_mad_u32_u24 v2, v2, s5, v10
	ds_read_b128 v[2:5], v2
	v_add_u32_e32 v20, s18, v1
	s_movk_i32 s0, 0xc0
	v_cmp_gt_u32_e64 s[0:1], s0, v0
	s_waitcnt lgkmcnt(0)
	v_cvt_f32_f16_e32 v1, v2
	v_cvt_f32_f16_sdwa v10, v2 dst_sel:DWORD dst_unused:UNUSED_PAD src0_sel:WORD_1
	v_cvt_f32_f16_e32 v12, v3
	v_cvt_f32_f16_sdwa v13, v3 dst_sel:DWORD dst_unused:UNUSED_PAD src0_sel:WORD_1
	v_cvt_f32_f16_e32 v14, v4
	v_cvt_f32_f16_sdwa v15, v4 dst_sel:DWORD dst_unused:UNUSED_PAD src0_sel:WORD_1
	v_cvt_f32_f16_e32 v16, v5
	v_cvt_f32_f16_sdwa v17, v5 dst_sel:DWORD dst_unused:UNUSED_PAD src0_sel:WORD_1
	v_max3_f32 v18, v1, 0, v10
	v_max3_f32 v18, v18, v12, v13
	v_max3_f32 v18, v18, v14, v15
	v_max3_f32 v18, v18, v16, v17
	v_cndmask_b32_e64 v0, v11, v20, s[0:1]
	v_cmp_gt_i32_e64 s[0:1], s4, v0
	v_mov_b32_dpp v19, v18 quad_perm:[1,0,3,2] row_mask:0xf bank_mask:0xf bound_ctrl:1
	v_max_f32_e32 v19, v19, v19
	v_max_f32_e32 v18, v18, v19
	s_nop 1
	v_mov_b32_dpp v19, v18 quad_perm:[2,3,0,1] row_mask:0xf bank_mask:0xf bound_ctrl:1
	v_max_f32_e32 v19, v19, v19
	v_max_f32_e32 v18, v18, v19
	s_nop 1
	v_mov_b32_dpp v19, v18 row_half_mirror row_mask:0xf bank_mask:0xf bound_ctrl:1
	v_max_f32_e32 v19, v19, v19
	v_max_f32_e32 v18, v18, v19
	s_nop 1
	v_mov_b32_dpp v19, v18 row_mirror row_mask:0xf bank_mask:0xf bound_ctrl:1
	s_and_saveexec_b64 s[2:3], s[0:1]
	s_cbranch_execz .LBB2_83
	v_max_f32_e32 v11, v19, v19
	v_max_f32_e32 v18, v18, v18
	v_max_f32_e32 v11, v18, v11
	v_rcp_f32_e32 v18, v11
	v_cmp_lt_f32_e64 s[0:1], 0, v11
	v_mul_f32_e32 v18, 0x437f0000, v18
	s_nop 0
	v_cndmask_b32_e64 v18, 0, v18, s[0:1]
	v_mul_f32_e32 v14, v18, v14
	v_mul_f32_e32 v1, v18, v1
	v_mul_f32_e32 v15, v18, v15
	v_rndne_f32_e32 v14, v14
	v_mul_f32_e32 v10, v18, v10
	v_rndne_f32_e32 v1, v1
	v_mul_f32_e32 v16, v18, v16
	v_rndne_f32_e32 v15, v15
	v_cvt_pk_u8_f32 v14, v14, 0, 0
	v_mul_f32_e32 v12, v18, v12
	v_rndne_f32_e32 v10, v10
	v_cvt_pk_u8_f32 v1, v1, 0, 0
	v_mul_f32_e32 v17, v18, v17
	v_rndne_f32_e32 v16, v16
	v_cvt_pk_u8_f32 v14, v15, 1, v14
	v_mul_f32_e32 v13, v18, v13
	v_rndne_f32_e32 v12, v12
	v_cvt_pk_u8_f32 v1, v10, 1, v1
	v_rndne_f32_e32 v17, v17
	v_cvt_pk_u8_f32 v14, v16, 2, v14
	v_rndne_f32_e32 v13, v13
	v_cvt_pk_u8_f32 v1, v12, 2, v1
	v_cvt_pk_u8_f32 v15, v17, 3, v14
	v_cvt_pk_u8_f32 v14, v13, 3, v1
	v_ashrrev_i32_e32 v1, 31, v0
	v_lshlrev_b64 v[16:17], 8, v[0:1]
	v_lshlrev_b64 v[12:13], 7, v[0:1]
	v_lshl_add_u64 v[8:9], v[8:9], 0, v[16:17]
	global_store_dwordx4 v[8:9], v[2:5], off sc1
	s_nop 1
	v_lshl_add_u64 v[2:3], v[6:7], 0, v[12:13]
	global_store_dwordx2 v[2:3], v[14:15], off
	s_and_b64 exec, exec, vcc
	s_cbranch_execz .LBB2_83
	v_lshl_add_u64 v[0:1], v[0:1], 2, s[14:15]
	v_mul_f32_e32 v2, 0x40808081, v11
	global_store_dword v[0:1], v2, off
